# v34 + P5 epilogue de-serialised: the bj=1 pair of residual-x loads issued together with the bj=0 pair (one HBM round trip per 16-row block instead of two)
# baseline (speedup 1.0000x reference)
; #define LAS __attribute__((address_space(3)))
; __device__ __forceinline__ unsigned cvt_pk_bf16(float lo, float hi) { unsigned r; asm volatile("v_cvt_pk_bf16_f32 %0, %1, %2" : "=v"(r) : "v"(lo), "v"(hi)); return r; }
;     __device__ __forceinline__ void operator()(const f32x4 (&acc)[2][2][4][2], const Unit& u, int wr, int wc, int fr, int fq) const {
;         const int lane = threadIdx.x & 63, b = u.row0 >> 12; LAS unsigned char* my = scr + (threadIdx.x >> 6) * 2304;
;         const int col0 = u.col0 + wc * 64 + 8 * fq, colw = u.col0 + wc * 64 + 8 * (lane & 7);
;         const float* gm = mod + (size_t)b * 12288 + 4096 + col0;
;         f32x4 gv[2][2];
; #pragma unroll
;         for (int bj = 0; bj < 2; ++bj)
; #pragma unroll
;             for (int n = 0; n < 2; ++n) gv[bj][n] = *(const f32x4*)(gm + bj * 32 + 4 * n) * (WSCALE_INV * PSCALE_INV);
; #pragma unroll
;         for (int ai = 0; ai < 2; ++ai)
; #pragma unroll
;             for (int m = 0; m < 4; ++m) {
;                 const float* xr = x + (size_t)(u.row0 + ai * 128 + wr * 64 + m * 16 + fr) * DM + col0;
; #pragma unroll
;                 for (int bj = 0; bj < 2; ++bj) { const f32x4 x0 = __builtin_nontemporal_load((const f32x4*)(xr + bj * 32)), x1 = __builtin_nontemporal_load((const f32x4*)(xr + bj * 32 + 4));
;                     const f32x4 v0 = x0 * DN_ALPHA + gv[bj][0] * acc[ai][bj][m][0], v1 = x1 * DN_ALPHA + gv[bj][1] * acc[ai][bj][m][1];
;                     u32x4 w; w.x = cvt_pk_bf16(v0[0], v0[1]); w.y = cvt_pk_bf16(v0[2], v0[3]); w.z = cvt_pk_bf16(v1[0], v1[1]); w.w = cvt_pk_bf16(v1[2], v1[3]);
;                     *(LAS u32x4*)(my + fr * 144 + bj * 64 + fq * 16) = w; }
; #pragma unroll
;                 for (int hh = 0; hh < 2; ++hh) { const int row = (lane >> 3) + 8 * hh; const u32x4 xx = *(const LAS u32x4*)(my + row * 144 + (lane & 7) * 16);
;                     *(u32x4*)(ZB + (size_t)(u.row0 + ai * 128 + wr * 64 + m * 16 + row) * DM + colw) = xx; }
.LBB0_705:
	v_bfe_u32 v163, v0, 3, 3
	v_or_b32_e32 v184, 8, v163
	s_or_b32 s6, s7, 32
	s_or_b32 s1, s7, 16
	v_or_b32_e32 v187, s6, v163
	v_or_b32_e32 v191, s6, v184
	s_sext_i32_i8 s6, s12
	s_nop 15
	s_nop 15
	s_or_b32 s13, s7, 48
	s_add_i32 s16, s7, 0x80
	s_add_i32 s17, s7, 0x90
	s_add_i32 s20, s7, 0xa0
	s_add_i32 s21, s7, 0xb0
	s_lshl_b32 s24, s47, 6
	v_mul_u32_u24_e32 v185, 0x90, v190
	v_or_b32_e32 v186, s1, v163
	v_or_b32_e32 v190, s1, v184
	s_lshl_b32 s1, s0, 8
	s_lshl_b32 s6, s6, 8
	s_add_u32 s12, s82, 0x4a600000
	v_and_b32_e32 v28, 7, v0
	s_movk_i32 s3, 0x90
	v_or_b32_e32 v182, s7, v163
	v_or_b32_e32 v33, s13, v163
	v_or_b32_e32 v31, s16, v163
	v_or_b32_e32 v29, s17, v163
	v_or_b32_e32 v26, s20, v163
	v_or_b32_e32 v24, s21, v184
	v_lshrrev_b32_e32 v188, 6, v0
	v_or_b32_e32 v183, s7, v184
	v_or_b32_e32 v162, s13, v184
	v_or_b32_e32 v32, s16, v184
	v_or_b32_e32 v30, s17, v184
	v_or_b32_e32 v27, s20, v184
	v_or_b32_e32 v25, s21, v163
	s_addc_u32 s13, s83, 0
	s_ashr_i32 s0, s0, 4
	s_or_b32 s17, s6, s24
	v_lshl_or_b32 v2, v189, 3, s17
	s_mul_hi_i32 s7, s0, 0xc000
	s_mul_i32 s0, s0, 0xc000
	s_add_u32 s6, s82, s0
	v_ashrrev_i32_e32 v3, 31, v2
	v_add_u32_e32 v14, s1, v171
	s_addc_u32 s7, s83, s7
	v_lshlrev_b64 v[2:3], 2, v[2:3]
	v_ashrrev_i32_e32 v15, 31, v14
	v_lshl_add_u64 v[12:13], s[6:7], 0, v[2:3]
	s_mov_b32 s0, 0x104000
	v_lshlrev_b64 v[4:5], 13, v[14:15]
	s_mov_b64 s[6:7], 0x104000
	v_lshl_add_u64 v[4:5], s[36:37], 0, v[4:5]
	v_add_co_u32_e32 v16, vcc, s0, v12
	v_lshl_add_u64 v[168:169], v[4:5], 0, v[2:3]
	s_nop 0
	v_addc_co_u32_e32 v17, vcc, 0, v13, vcc
	v_lshl_add_u64 v[12:13], v[12:13], 0, s[6:7]
	global_load_dwordx4 v[4:7], v[168:169], off offset:16 nt
	global_load_dwordx4 v[8:11], v[168:169], off nt
	global_load_dwordx4 v[20:23], v[12:13], off offset:16
	s_mov_b32 s16, 0x3b000000
	global_load_dwordx4 v[16:19], v[16:17], off
	s_mov_b32 s0, 0x3f9837f0
	global_load_dwordx4 v[164:167], v[12:13], off offset:144
	global_load_dwordx4 v[172:175], v[12:13], off offset:128
	global_load_dwordx4 v[240:243], v[168:169], off offset:128 nt
	global_load_dwordx4 v[244:247], v[168:169], off offset:144 nt
	s_add_i32 s7, 0, 0x20000
	s_movk_i32 s6, 0x900
	v_mov_b32_e32 v15, s7
	v_mad_u32_u24 v15, v188, s6, v15
	v_add3_u32 v1, v15, v185, v1
	v_add_u32_e32 v32, s1, v32
	v_add_u32_e32 v30, s1, v30
	v_add_u32_e32 v26, s1, v26
	v_add_u32_e32 v24, s1, v24
	v_readlane_b32 s56, v255, 7
	s_waitcnt vmcnt(2)
	v_pk_mul_f32 v[180:181], v[6:7], s[0:1] op_sel_hi:[1,0]
	v_pk_mul_f32 v[176:177], v[10:11], s[0:1] op_sel_hi:[1,0]
	v_pk_mul_f32 v[178:179], v[8:9], s[0:1] op_sel_hi:[1,0]
	v_pk_mul_f32 v[4:5], v[4:5], s[0:1] op_sel_hi:[1,0]
	v_pk_mul_f32 v[10:11], v[18:19], s[16:17] op_sel_hi:[1,0]
	v_pk_mul_f32 v[12:13], v[16:17], s[16:17] op_sel_hi:[1,0]
	v_pk_mul_f32 v[6:7], v[22:23], s[16:17] op_sel_hi:[1,0]
	v_pk_mul_f32 v[8:9], v[20:21], s[16:17] op_sel_hi:[1,0]
	v_pk_fma_f32 v[16:17], v[160:161], v[10:11], v[176:177]
	v_pk_fma_f32 v[18:19], v[158:159], v[12:13], v[178:179]
	v_pk_fma_f32 v[20:21], v[156:157], v[6:7], v[180:181]
	v_pk_fma_f32 v[4:5], v[154:155], v[8:9], v[4:5]
	v_cvt_pk_bf16_f32 v154, v18, v19
	v_cvt_pk_bf16_f32 v155, v16, v17
	v_add_u32_e32 v16, s1, v183
	v_cvt_pk_bf16_f32 v156, v4, v5
	v_cvt_pk_bf16_f32 v157, v20, v21
	s_waitcnt vmcnt(0)
	v_mov_b64_e32 v[158:159], v[240:241]
	v_mov_b64_e32 v[160:161], v[242:243]
	v_mov_b64_e32 v[176:177], v[244:245]
	v_mov_b64_e32 v[178:179], v[246:247]
	v_add_u32_e32 v4, s1, v182
	v_lshl_or_b32 v18, v28, 3, s17
	v_ashrrev_i32_e32 v5, 31, v4
	v_ashrrev_i32_e32 v17, 31, v16
	v_add_u32_e32 v20, 16, v14
	v_ashrrev_i32_e32 v19, 31, v18
	v_lshlrev_b64 v[4:5], 12, v[4:5]
	v_lshlrev_b64 v[16:17], 12, v[16:17]
	v_ashrrev_i32_e32 v21, 31, v20
	v_lshl_add_u64 v[22:23], s[12:13], 0, v[4:5]
	v_lshlrev_b64 v[4:5], 1, v[18:19]
	v_lshl_add_u64 v[168:169], s[12:13], 0, v[16:17]
	v_lshl_add_u32 v16, v28, 4, v15
	v_lshlrev_b64 v[180:181], 13, v[20:21]
	v_lshl_add_u64 v[182:183], v[22:23], 0, v[4:5]
	v_mad_u32_u24 v15, v163, s3, v16
	v_mad_u32_u24 v28, v184, s3, v16
	v_pk_mul_f32 v[16:17], v[174:175], s[16:17] op_sel_hi:[1,0]
	v_pk_mul_f32 v[20:21], v[166:167], s[16:17] op_sel_hi:[1,0]
	v_pk_mul_f32 v[22:23], v[164:165], s[16:17] op_sel_hi:[1,0]
	ds_write_b128 v1, v[154:157]
	v_pk_mul_f32 v[18:19], v[172:173], s[16:17] op_sel_hi:[1,0]
	s_waitcnt vmcnt(1)
	v_pk_mul_f32 v[154:155], v[160:161], s[0:1] op_sel_hi:[1,0]
	v_pk_mul_f32 v[156:157], v[158:159], s[0:1] op_sel_hi:[1,0]
	s_waitcnt vmcnt(0)
	v_pk_mul_f32 v[158:159], v[178:179], s[0:1] op_sel_hi:[1,0]
	v_pk_mul_f32 v[160:161], v[176:177], s[0:1] op_sel_hi:[1,0]
	v_pk_fma_f32 v[152:153], v[152:153], v[16:17], v[154:155]
	v_pk_fma_f32 v[154:155], v[148:149], v[20:21], v[158:159]
	v_pk_fma_f32 v[148:149], v[146:147], v[22:23], v[160:161]
	v_pk_fma_f32 v[150:151], v[150:151], v[18:19], v[156:157]
	v_lshl_add_u64 v[156:157], s[36:37], 0, v[180:181]
	v_cvt_pk_bf16_f32 v146, v150, v151
	v_cvt_pk_bf16_f32 v147, v152, v153
	v_cvt_pk_bf16_f32 v148, v148, v149
	v_cvt_pk_bf16_f32 v149, v154, v155
	ds_write_b128 v1, v[146:149] offset:64
	ds_read_b128 v[146:149], v15
	ds_read_b128 v[150:153], v28
	v_lshl_add_u64 v[154:155], v[168:169], 0, v[4:5]
	v_lshl_add_u64 v[156:157], v[156:157], 0, v[2:3]
	s_waitcnt lgkmcnt(1)
	global_store_dwordx4 v[182:183], v[146:149], off sc0 sc1
	s_waitcnt lgkmcnt(0)
	global_store_dwordx4 v[154:155], v[150:153], off sc0 sc1
	global_load_dwordx4 v[146:149], v[156:157], off nt
	s_nop 0
	global_load_dwordx4 v[150:153], v[156:157], off offset:16 nt
	global_load_dwordx4 v[240:243], v[156:157], off offset:128 nt
	global_load_dwordx4 v[244:247], v[156:157], off offset:144 nt
	v_add_u32_e32 v154, 32, v14
	v_ashrrev_i32_e32 v155, 31, v154
	v_lshlrev_b64 v[154:155], 13, v[154:155]
	s_waitcnt vmcnt(3)
; #define LAS __attribute__((address_space(3)))
; __device__ __forceinline__ unsigned cvt_pk_bf16(float lo, float hi) { unsigned r; asm volatile("v_cvt_pk_bf16_f32 %0, %1, %2" : "=v"(r) : "v"(lo), "v"(hi)); return r; }
;     __device__ __forceinline__ void operator()(const f32x4 (&acc)[2][2][4][2], const Unit& u, int wr, int wc, int fr, int fq) const {
;     ...
;             for (int m = 0; m < 4; ++m) {
;                 const float* xr = x + (size_t)(u.row0 + ai * 128 + wr * 64 + m * 16 + fr) * DM + col0;
; #pragma unroll
;                 for (int bj = 0; bj < 2; ++bj) { const f32x4 x0 = __builtin_nontemporal_load((const f32x4*)(xr + bj * 32)), x1 = __builtin_nontemporal_load((const f32x4*)(xr + bj * 32 + 4));
;                     const f32x4 v0 = x0 * DN_ALPHA + gv[bj][0] * acc[ai][bj][m][0], v1 = x1 * DN_ALPHA + gv[bj][1] * acc[ai][bj][m][1];
;                     u32x4 w; w.x = cvt_pk_bf16(v0[0], v0[1]); w.y = cvt_pk_bf16(v0[2], v0[3]); w.z = cvt_pk_bf16(v1[0], v1[1]); w.w = cvt_pk_bf16(v1[2], v1[3]);
;                     *(LAS u32x4*)(my + fr * 144 + bj * 64 + fq * 16) = w; }
; #pragma unroll
;                 for (int hh = 0; hh < 2; ++hh) { const int row = (lane >> 3) + 8 * hh; const u32x4 xx = *(const LAS u32x4*)(my + row * 144 + (lane & 7) * 16);
;                     *(u32x4*)(ZB + (size_t)(u.row0 + ai * 128 + wr * 64 + m * 16 + row) * DM + colw) = xx; }
	v_pk_mul_f32 v[148:149], v[148:149], s[0:1] op_sel_hi:[1,0]
	v_pk_mul_f32 v[146:147], v[146:147], s[0:1] op_sel_hi:[1,0]
	s_waitcnt vmcnt(2)
	v_pk_mul_f32 v[152:153], v[152:153], s[0:1] op_sel_hi:[1,0]
	v_pk_mul_f32 v[150:151], v[150:151], s[0:1] op_sel_hi:[1,0]
	v_pk_fma_f32 v[144:145], v[144:145], v[10:11], v[148:149]
	v_pk_fma_f32 v[142:143], v[142:143], v[12:13], v[146:147]
	v_pk_fma_f32 v[146:147], v[140:141], v[6:7], v[152:153]
	v_pk_fma_f32 v[140:141], v[138:139], v[8:9], v[150:151]
	v_cvt_pk_bf16_f32 v138, v142, v143
	v_cvt_pk_bf16_f32 v139, v144, v145
	v_add_u32_e32 v150, s1, v186
	v_cvt_pk_bf16_f32 v140, v140, v141
	v_cvt_pk_bf16_f32 v141, v146, v147
	s_waitcnt vmcnt(0)
	v_mov_b64_e32 v[142:143], v[240:241]
	v_mov_b64_e32 v[144:145], v[242:243]
	v_mov_b64_e32 v[146:147], v[244:245]
	v_mov_b64_e32 v[148:149], v[246:247]
	ds_write_b128 v1, v[138:141]
	v_add_u32_e32 v152, s1, v190
	v_ashrrev_i32_e32 v151, 31, v150
	v_ashrrev_i32_e32 v153, 31, v152
	v_lshlrev_b64 v[150:151], 12, v[150:151]
	v_lshlrev_b64 v[152:153], 12, v[152:153]
	v_lshl_add_u64 v[150:151], s[12:13], 0, v[150:151]
	v_lshl_add_u64 v[152:153], s[12:13], 0, v[152:153]
	v_lshl_add_u64 v[150:151], v[150:151], 0, v[4:5]
	s_waitcnt vmcnt(1)
	v_pk_mul_f32 v[138:139], v[144:145], s[0:1] op_sel_hi:[1,0]
	v_pk_mul_f32 v[140:141], v[142:143], s[0:1] op_sel_hi:[1,0]
	s_waitcnt vmcnt(0)
	v_pk_mul_f32 v[142:143], v[148:149], s[0:1] op_sel_hi:[1,0]
	v_pk_mul_f32 v[144:145], v[146:147], s[0:1] op_sel_hi:[1,0]
	v_pk_fma_f32 v[136:137], v[136:137], v[16:17], v[138:139]
	v_pk_fma_f32 v[138:139], v[132:133], v[20:21], v[142:143]
	v_pk_fma_f32 v[132:133], v[130:131], v[22:23], v[144:145]
	v_pk_fma_f32 v[134:135], v[134:135], v[18:19], v[140:141]
	v_lshl_add_u64 v[140:141], s[36:37], 0, v[154:155]
	v_cvt_pk_bf16_f32 v130, v134, v135
	v_cvt_pk_bf16_f32 v131, v136, v137
	v_cvt_pk_bf16_f32 v132, v132, v133
	v_cvt_pk_bf16_f32 v133, v138, v139
	ds_write_b128 v1, v[130:133] offset:64
	ds_read_b128 v[130:133], v15
	ds_read_b128 v[134:137], v28
	v_lshl_add_u64 v[138:139], v[152:153], 0, v[4:5]
	v_lshl_add_u64 v[140:141], v[140:141], 0, v[2:3]
	s_waitcnt lgkmcnt(1)
	global_store_dwordx4 v[150:151], v[130:133], off sc0 sc1
	s_waitcnt lgkmcnt(0)
	global_store_dwordx4 v[138:139], v[134:137], off sc0 sc1
	global_load_dwordx4 v[130:133], v[140:141], off nt
	s_nop 0
	global_load_dwordx4 v[134:137], v[140:141], off offset:16 nt
	global_load_dwordx4 v[240:243], v[140:141], off offset:128 nt
	global_load_dwordx4 v[244:247], v[140:141], off offset:144 nt
	v_add_u32_e32 v138, 48, v14
	v_ashrrev_i32_e32 v139, 31, v138
	v_lshlrev_b64 v[138:139], 13, v[138:139]
	s_waitcnt vmcnt(3)
	v_pk_mul_f32 v[132:133], v[132:133], s[0:1] op_sel_hi:[1,0]
	v_pk_mul_f32 v[130:131], v[130:131], s[0:1] op_sel_hi:[1,0]
	s_waitcnt vmcnt(2)
	v_pk_mul_f32 v[136:137], v[136:137], s[0:1] op_sel_hi:[1,0]
	v_pk_mul_f32 v[134:135], v[134:135], s[0:1] op_sel_hi:[1,0]
	v_pk_fma_f32 v[128:129], v[128:129], v[10:11], v[132:133]
	v_pk_fma_f32 v[126:127], v[126:127], v[12:13], v[130:131]
	v_pk_fma_f32 v[130:131], v[124:125], v[6:7], v[136:137]
	v_pk_fma_f32 v[124:125], v[122:123], v[8:9], v[134:135]
	v_cvt_pk_bf16_f32 v122, v126, v127
	v_cvt_pk_bf16_f32 v123, v128, v129
	v_add_u32_e32 v134, s1, v187
	v_cvt_pk_bf16_f32 v124, v124, v125
	v_cvt_pk_bf16_f32 v125, v130, v131
	s_waitcnt vmcnt(0)
	v_mov_b64_e32 v[126:127], v[240:241]
	v_mov_b64_e32 v[128:129], v[242:243]
	v_mov_b64_e32 v[130:131], v[244:245]
	v_mov_b64_e32 v[132:133], v[246:247]
	ds_write_b128 v1, v[122:125]
	v_add_u32_e32 v136, s1, v191
	v_ashrrev_i32_e32 v135, 31, v134
	v_ashrrev_i32_e32 v137, 31, v136
	v_lshlrev_b64 v[134:135], 12, v[134:135]
	v_lshlrev_b64 v[136:137], 12, v[136:137]
	v_lshl_add_u64 v[134:135], s[12:13], 0, v[134:135]
	v_lshl_add_u64 v[136:137], s[12:13], 0, v[136:137]
	v_lshl_add_u64 v[134:135], v[134:135], 0, v[4:5]
	s_waitcnt vmcnt(1)
	v_pk_mul_f32 v[122:123], v[128:129], s[0:1] op_sel_hi:[1,0]
	v_pk_mul_f32 v[124:125], v[126:127], s[0:1] op_sel_hi:[1,0]
	s_waitcnt vmcnt(0)
	v_pk_mul_f32 v[126:127], v[132:133], s[0:1] op_sel_hi:[1,0]
	v_pk_mul_f32 v[128:129], v[130:131], s[0:1] op_sel_hi:[1,0]
	v_pk_fma_f32 v[120:121], v[120:121], v[16:17], v[122:123]
	v_pk_fma_f32 v[122:123], v[116:117], v[20:21], v[126:127]
	v_pk_fma_f32 v[116:117], v[114:115], v[22:23], v[128:129]
	v_pk_fma_f32 v[118:119], v[118:119], v[18:19], v[124:125]
	v_lshl_add_u64 v[124:125], s[36:37], 0, v[138:139]
	v_cvt_pk_bf16_f32 v114, v118, v119
	v_cvt_pk_bf16_f32 v115, v120, v121
	v_cvt_pk_bf16_f32 v116, v116, v117
	v_cvt_pk_bf16_f32 v117, v122, v123
	ds_write_b128 v1, v[114:117] offset:64
	ds_read_b128 v[114:117], v15
	ds_read_b128 v[118:121], v28
	v_lshl_add_u64 v[122:123], v[136:137], 0, v[4:5]
	v_lshl_add_u64 v[124:125], v[124:125], 0, v[2:3]
	s_waitcnt lgkmcnt(1)
	global_store_dwordx4 v[134:135], v[114:117], off sc0 sc1
	s_waitcnt lgkmcnt(0)
	global_store_dwordx4 v[122:123], v[118:121], off sc0 sc1
	global_load_dwordx4 v[114:117], v[124:125], off nt
	s_nop 0
	global_load_dwordx4 v[118:121], v[124:125], off offset:16 nt
	global_load_dwordx4 v[240:243], v[124:125], off offset:128 nt
	global_load_dwordx4 v[244:247], v[124:125], off offset:144 nt
	v_add_u32_e32 v122, 0x80, v14
	v_ashrrev_i32_e32 v123, 31, v122
	v_lshlrev_b64 v[122:123], 13, v[122:123]
	s_waitcnt vmcnt(3)
	v_pk_mul_f32 v[116:117], v[116:117], s[0:1] op_sel_hi:[1,0]
	v_pk_mul_f32 v[114:115], v[114:115], s[0:1] op_sel_hi:[1,0]
	s_waitcnt vmcnt(2)
; #define LAS __attribute__((address_space(3)))
; __device__ __forceinline__ unsigned cvt_pk_bf16(float lo, float hi) { unsigned r; asm volatile("v_cvt_pk_bf16_f32 %0, %1, %2" : "=v"(r) : "v"(lo), "v"(hi)); return r; }
;     __device__ __forceinline__ void operator()(const f32x4 (&acc)[2][2][4][2], const Unit& u, int wr, int wc, int fr, int fq) const {
;     ...
;             for (int m = 0; m < 4; ++m) {
;                 const float* xr = x + (size_t)(u.row0 + ai * 128 + wr * 64 + m * 16 + fr) * DM + col0;
; #pragma unroll
;                 for (int bj = 0; bj < 2; ++bj) { const f32x4 x0 = __builtin_nontemporal_load((const f32x4*)(xr + bj * 32)), x1 = __builtin_nontemporal_load((const f32x4*)(xr + bj * 32 + 4));
;                     const f32x4 v0 = x0 * DN_ALPHA + gv[bj][0] * acc[ai][bj][m][0], v1 = x1 * DN_ALPHA + gv[bj][1] * acc[ai][bj][m][1];
;                     u32x4 w; w.x = cvt_pk_bf16(v0[0], v0[1]); w.y = cvt_pk_bf16(v0[2], v0[3]); w.z = cvt_pk_bf16(v1[0], v1[1]); w.w = cvt_pk_bf16(v1[2], v1[3]);
;                     *(LAS u32x4*)(my + fr * 144 + bj * 64 + fq * 16) = w; }
; #pragma unroll
;                 for (int hh = 0; hh < 2; ++hh) { const int row = (lane >> 3) + 8 * hh; const u32x4 xx = *(const LAS u32x4*)(my + row * 144 + (lane & 7) * 16);
;                     *(u32x4*)(ZB + (size_t)(u.row0 + ai * 128 + wr * 64 + m * 16 + row) * DM + colw) = xx; }
	v_pk_mul_f32 v[120:121], v[120:121], s[0:1] op_sel_hi:[1,0]
	v_pk_mul_f32 v[118:119], v[118:119], s[0:1] op_sel_hi:[1,0]
	v_pk_fma_f32 v[112:113], v[112:113], v[10:11], v[116:117]
	v_pk_fma_f32 v[110:111], v[110:111], v[12:13], v[114:115]
	v_pk_fma_f32 v[114:115], v[108:109], v[6:7], v[120:121]
	v_pk_fma_f32 v[108:109], v[106:107], v[8:9], v[118:119]
	v_cvt_pk_bf16_f32 v106, v110, v111
	v_cvt_pk_bf16_f32 v107, v112, v113
	v_add_u32_e32 v118, s1, v33
	v_cvt_pk_bf16_f32 v108, v108, v109
	v_cvt_pk_bf16_f32 v109, v114, v115
	s_waitcnt vmcnt(0)
	v_mov_b64_e32 v[110:111], v[240:241]
	v_mov_b64_e32 v[112:113], v[242:243]
	v_mov_b64_e32 v[114:115], v[244:245]
	v_mov_b64_e32 v[116:117], v[246:247]
	ds_write_b128 v1, v[106:109]
	v_add_u32_e32 v120, s1, v162
	v_ashrrev_i32_e32 v119, 31, v118
	v_ashrrev_i32_e32 v121, 31, v120
	v_lshlrev_b64 v[118:119], 12, v[118:119]
	v_lshlrev_b64 v[120:121], 12, v[120:121]
	v_lshl_add_u64 v[118:119], s[12:13], 0, v[118:119]
	v_lshl_add_u64 v[120:121], s[12:13], 0, v[120:121]
	v_lshl_add_u64 v[118:119], v[118:119], 0, v[4:5]
	v_ashrrev_i32_e32 v33, 31, v32
	v_lshlrev_b64 v[32:33], 12, v[32:33]
	v_lshl_add_u64 v[32:33], s[12:13], 0, v[32:33]
	v_lshl_add_u64 v[32:33], v[32:33], 0, v[4:5]
	s_waitcnt vmcnt(1)
	v_pk_mul_f32 v[106:107], v[112:113], s[0:1] op_sel_hi:[1,0]
	v_pk_mul_f32 v[108:109], v[110:111], s[0:1] op_sel_hi:[1,0]
	s_waitcnt vmcnt(0)
	v_pk_mul_f32 v[110:111], v[116:117], s[0:1] op_sel_hi:[1,0]
	v_pk_mul_f32 v[112:113], v[114:115], s[0:1] op_sel_hi:[1,0]
	v_pk_fma_f32 v[104:105], v[104:105], v[16:17], v[106:107]
	v_pk_fma_f32 v[106:107], v[100:101], v[20:21], v[110:111]
	v_pk_fma_f32 v[100:101], v[98:99], v[22:23], v[112:113]
	v_pk_fma_f32 v[102:103], v[102:103], v[18:19], v[108:109]
	v_lshl_add_u64 v[108:109], s[36:37], 0, v[122:123]
	v_cvt_pk_bf16_f32 v98, v102, v103
	v_cvt_pk_bf16_f32 v99, v104, v105
	v_cvt_pk_bf16_f32 v100, v100, v101
	v_cvt_pk_bf16_f32 v101, v106, v107
	ds_write_b128 v1, v[98:101] offset:64
	ds_read_b128 v[98:101], v15
	ds_read_b128 v[102:105], v28
	v_lshl_add_u64 v[106:107], v[120:121], 0, v[4:5]
	v_lshl_add_u64 v[108:109], v[108:109], 0, v[2:3]
	s_waitcnt lgkmcnt(1)
	global_store_dwordx4 v[118:119], v[98:101], off sc0 sc1
	s_waitcnt lgkmcnt(0)
	global_store_dwordx4 v[106:107], v[102:105], off sc0 sc1
	global_load_dwordx4 v[98:101], v[108:109], off nt
	s_nop 0
	global_load_dwordx4 v[102:105], v[108:109], off offset:16 nt
	global_load_dwordx4 v[240:243], v[108:109], off offset:128 nt
	global_load_dwordx4 v[244:247], v[108:109], off offset:144 nt
	s_waitcnt vmcnt(3)
	v_pk_mul_f32 v[100:101], v[100:101], s[0:1] op_sel_hi:[1,0]
	v_pk_mul_f32 v[98:99], v[98:99], s[0:1] op_sel_hi:[1,0]
	s_waitcnt vmcnt(2)
	v_pk_mul_f32 v[104:105], v[104:105], s[0:1] op_sel_hi:[1,0]
	v_pk_mul_f32 v[102:103], v[102:103], s[0:1] op_sel_hi:[1,0]
	v_pk_fma_f32 v[96:97], v[96:97], v[10:11], v[100:101]
	v_pk_fma_f32 v[94:95], v[94:95], v[12:13], v[98:99]
	v_pk_fma_f32 v[98:99], v[92:93], v[6:7], v[104:105]
	v_pk_fma_f32 v[92:93], v[90:91], v[8:9], v[102:103]
	v_cvt_pk_bf16_f32 v90, v94, v95
	v_cvt_pk_bf16_f32 v91, v96, v97
	v_add_u32_e32 v102, s1, v31
	v_cvt_pk_bf16_f32 v92, v92, v93
	v_cvt_pk_bf16_f32 v93, v98, v99
	s_waitcnt vmcnt(0)
	v_mov_b64_e32 v[94:95], v[240:241]
	v_mov_b64_e32 v[96:97], v[242:243]
	v_mov_b64_e32 v[98:99], v[244:245]
	v_mov_b64_e32 v[100:101], v[246:247]
	ds_write_b128 v1, v[90:93]
	v_ashrrev_i32_e32 v103, 31, v102
	v_add_u32_e32 v104, 0x90, v14
	v_lshlrev_b64 v[102:103], 12, v[102:103]
	v_ashrrev_i32_e32 v105, 31, v104
	v_lshl_add_u64 v[102:103], s[12:13], 0, v[102:103]
	v_lshlrev_b64 v[104:105], 13, v[104:105]
	v_lshl_add_u64 v[102:103], v[102:103], 0, v[4:5]
	v_ashrrev_i32_e32 v31, 31, v30
	v_lshlrev_b64 v[30:31], 12, v[30:31]
	s_waitcnt vmcnt(1)
	v_pk_mul_f32 v[90:91], v[96:97], s[0:1] op_sel_hi:[1,0]
	v_pk_mul_f32 v[92:93], v[94:95], s[0:1] op_sel_hi:[1,0]
	s_waitcnt vmcnt(0)
	v_pk_mul_f32 v[94:95], v[100:101], s[0:1] op_sel_hi:[1,0]
	v_pk_mul_f32 v[96:97], v[98:99], s[0:1] op_sel_hi:[1,0]
	v_pk_fma_f32 v[88:89], v[88:89], v[16:17], v[90:91]
	v_pk_fma_f32 v[90:91], v[84:85], v[20:21], v[94:95]
	v_pk_fma_f32 v[84:85], v[82:83], v[22:23], v[96:97]
	v_pk_fma_f32 v[86:87], v[86:87], v[18:19], v[92:93]
	s_nop 0
	v_cvt_pk_bf16_f32 v82, v86, v87
	v_cvt_pk_bf16_f32 v83, v88, v89
	v_cvt_pk_bf16_f32 v84, v84, v85
	v_cvt_pk_bf16_f32 v85, v90, v91
	ds_write_b128 v1, v[82:85] offset:64
	ds_read_b128 v[82:85], v15
	ds_read_b128 v[86:89], v28
	v_lshl_add_u64 v[90:91], s[36:37], 0, v[104:105]
	v_lshl_add_u64 v[90:91], v[90:91], 0, v[2:3]
	s_waitcnt lgkmcnt(1)
	global_store_dwordx4 v[102:103], v[82:85], off sc0 sc1
	s_waitcnt lgkmcnt(0)
	global_store_dwordx4 v[32:33], v[86:89], off sc0 sc1
	global_load_dwordx4 v[82:85], v[90:91], off nt
	s_nop 0
	global_load_dwordx4 v[86:89], v[90:91], off offset:16 nt
	global_load_dwordx4 v[240:243], v[90:91], off offset:128 nt
	global_load_dwordx4 v[244:247], v[90:91], off offset:144 nt
	s_waitcnt vmcnt(3)
	v_pk_mul_f32 v[32:33], v[84:85], s[0:1] op_sel_hi:[1,0]
	v_pk_mul_f32 v[82:83], v[82:83], s[0:1] op_sel_hi:[1,0]
	s_waitcnt vmcnt(2)
	v_pk_mul_f32 v[84:85], v[88:89], s[0:1] op_sel_hi:[1,0]
	v_pk_mul_f32 v[86:87], v[86:87], s[0:1] op_sel_hi:[1,0]
	v_pk_fma_f32 v[32:33], v[80:81], v[10:11], v[32:33]
	v_pk_fma_f32 v[78:79], v[78:79], v[12:13], v[82:83]
	v_pk_fma_f32 v[80:81], v[76:77], v[6:7], v[84:85]
	v_pk_fma_f32 v[76:77], v[74:75], v[8:9], v[86:87]
	v_cvt_pk_bf16_f32 v74, v78, v79
	v_cvt_pk_bf16_f32 v75, v32, v33
	v_add_u32_e32 v32, s1, v29
	v_cvt_pk_bf16_f32 v76, v76, v77
	v_cvt_pk_bf16_f32 v77, v80, v81
	s_waitcnt vmcnt(0)
; #define LAS __attribute__((address_space(3)))
; __device__ __forceinline__ unsigned cvt_pk_bf16(float lo, float hi) { unsigned r; asm volatile("v_cvt_pk_bf16_f32 %0, %1, %2" : "=v"(r) : "v"(lo), "v"(hi)); return r; }
; #define PG8_WAIT_V(n) asm volatile("s_waitcnt vmcnt(" #n ")" ::: "memory")
; #define PG8_BAR __builtin_amdgcn_s_barrier()
; template <class Epi, class Sched, bool GATHER, bool F8 = false>
; __device__ __forceinline__ void gemm_phase(LAS unsigned char* lds, const int K, const Sched& S, const Epi& E) {
;     ...
;     PG8_WAIT_V(0);
;     PG8_BAR;
;     __device__ __forceinline__ void operator()(const f32x4 (&acc)[2][2][4][2], const Unit& u, int wr, int wc, int fr, int fq) const {
;     ...
;             for (int m = 0; m < 4; ++m) {
;                 const float* xr = x + (size_t)(u.row0 + ai * 128 + wr * 64 + m * 16 + fr) * DM + col0;
; #pragma unroll
;                 for (int bj = 0; bj < 2; ++bj) { const f32x4 x0 = __builtin_nontemporal_load((const f32x4*)(xr + bj * 32)), x1 = __builtin_nontemporal_load((const f32x4*)(xr + bj * 32 + 4));
;                     const f32x4 v0 = x0 * DN_ALPHA + gv[bj][0] * acc[ai][bj][m][0], v1 = x1 * DN_ALPHA + gv[bj][1] * acc[ai][bj][m][1];
;                     u32x4 w; w.x = cvt_pk_bf16(v0[0], v0[1]); w.y = cvt_pk_bf16(v0[2], v0[3]); w.z = cvt_pk_bf16(v1[0], v1[1]); w.w = cvt_pk_bf16(v1[2], v1[3]);
;                     *(LAS u32x4*)(my + fr * 144 + bj * 64 + fq * 16) = w; }
; #pragma unroll
;                 for (int hh = 0; hh < 2; ++hh) { const int row = (lane >> 3) + 8 * hh; const u32x4 xx = *(const LAS u32x4*)(my + row * 144 + (lane & 7) * 16);
;                     *(u32x4*)(ZB + (size_t)(u.row0 + ai * 128 + wr * 64 + m * 16 + row) * DM + colw) = xx; }
	v_mov_b64_e32 v[78:79], v[240:241]
	v_mov_b64_e32 v[80:81], v[242:243]
	v_mov_b64_e32 v[82:83], v[244:245]
	v_mov_b64_e32 v[84:85], v[246:247]
	v_ashrrev_i32_e32 v33, 31, v32
	v_lshlrev_b64 v[32:33], 12, v[32:33]
	v_lshl_add_u64 v[32:33], s[12:13], 0, v[32:33]
	v_lshl_add_u64 v[88:89], s[12:13], 0, v[30:31]
	v_lshl_add_u64 v[90:91], v[32:33], 0, v[4:5]
	ds_write_b128 v1, v[74:77]
	v_add_u32_e32 v86, 0xa0, v14
	v_ashrrev_i32_e32 v87, 31, v86
	v_lshlrev_b64 v[86:87], 13, v[86:87]
	s_waitcnt vmcnt(1)
	v_pk_mul_f32 v[30:31], v[80:81], s[0:1] op_sel_hi:[1,0]
	v_pk_mul_f32 v[32:33], v[78:79], s[0:1] op_sel_hi:[1,0]
	s_waitcnt vmcnt(0)
	v_pk_mul_f32 v[76:77], v[82:83], s[0:1] op_sel_hi:[1,0]
	v_pk_mul_f32 v[74:75], v[84:85], s[0:1] op_sel_hi:[1,0]
	v_pk_fma_f32 v[72:73], v[72:73], v[16:17], v[30:31]
	v_pk_fma_f32 v[30:31], v[70:71], v[18:19], v[32:33]
	v_pk_fma_f32 v[32:33], v[66:67], v[22:23], v[76:77]
	v_pk_fma_f32 v[68:69], v[68:69], v[20:21], v[74:75]
	v_cvt_pk_bf16_f32 v30, v30, v31
	v_cvt_pk_bf16_f32 v31, v72, v73
	v_cvt_pk_bf16_f32 v32, v32, v33
	v_lshl_add_u64 v[72:73], s[36:37], 0, v[86:87]
	v_cvt_pk_bf16_f32 v33, v68, v69
	ds_write_b128 v1, v[30:33] offset:64
	ds_read_b128 v[30:33], v15
	ds_read_b128 v[66:69], v28
	v_lshl_add_u64 v[70:71], v[88:89], 0, v[4:5]
	v_lshl_add_u64 v[72:73], v[72:73], 0, v[2:3]
	s_waitcnt lgkmcnt(1)
	global_store_dwordx4 v[90:91], v[30:33], off sc0 sc1
	s_waitcnt lgkmcnt(0)
	global_store_dwordx4 v[70:71], v[66:69], off sc0 sc1
	global_load_dwordx4 v[30:33], v[72:73], off nt
	s_nop 0
	global_load_dwordx4 v[66:69], v[72:73], off offset:16 nt
	global_load_dwordx4 v[240:243], v[72:73], off offset:128 nt
	global_load_dwordx4 v[244:247], v[72:73], off offset:144 nt
	s_waitcnt vmcnt(3)
	v_pk_mul_f32 v[32:33], v[32:33], s[0:1] op_sel_hi:[1,0]
	v_pk_mul_f32 v[30:31], v[30:31], s[0:1] op_sel_hi:[1,0]
	s_waitcnt vmcnt(2)
	v_pk_mul_f32 v[68:69], v[68:69], s[0:1] op_sel_hi:[1,0]
	v_pk_mul_f32 v[66:67], v[66:67], s[0:1] op_sel_hi:[1,0]
	v_pk_fma_f32 v[32:33], v[64:65], v[10:11], v[32:33]
	v_pk_fma_f32 v[30:31], v[62:63], v[12:13], v[30:31]
	v_pk_fma_f32 v[60:61], v[60:61], v[6:7], v[68:69]
	v_pk_fma_f32 v[58:59], v[58:59], v[8:9], v[66:67]
	v_cvt_pk_bf16_f32 v30, v30, v31
	v_cvt_pk_bf16_f32 v31, v32, v33
	v_add_u32_e32 v66, s1, v27
	v_cvt_pk_bf16_f32 v32, v58, v59
	v_cvt_pk_bf16_f32 v33, v60, v61
	s_waitcnt vmcnt(0)
	v_mov_b64_e32 v[58:59], v[240:241]
	v_mov_b64_e32 v[60:61], v[242:243]
	v_mov_b64_e32 v[62:63], v[244:245]
	v_mov_b64_e32 v[64:65], v[246:247]
	ds_write_b128 v1, v[30:33]
	v_ashrrev_i32_e32 v27, 31, v26
	v_add_u32_e32 v68, 0xb0, v14
	v_ashrrev_i32_e32 v67, 31, v66
	v_lshlrev_b64 v[26:27], 12, v[26:27]
	v_ashrrev_i32_e32 v69, 31, v68
	v_lshlrev_b64 v[66:67], 12, v[66:67]
	v_lshl_add_u64 v[26:27], s[12:13], 0, v[26:27]
	v_lshlrev_b64 v[68:69], 13, v[68:69]
	v_lshl_add_u64 v[66:67], s[12:13], 0, v[66:67]
	v_lshl_add_u64 v[26:27], v[26:27], 0, v[4:5]
	s_waitcnt vmcnt(1)
	v_pk_mul_f32 v[30:31], v[60:61], s[0:1] op_sel_hi:[1,0]
	v_pk_mul_f32 v[32:33], v[58:59], s[0:1] op_sel_hi:[1,0]
	s_waitcnt vmcnt(0)
	v_pk_mul_f32 v[60:61], v[62:63], s[0:1] op_sel_hi:[1,0]
	v_pk_mul_f32 v[58:59], v[64:65], s[0:1] op_sel_hi:[1,0]
	v_pk_fma_f32 v[56:57], v[56:57], v[16:17], v[30:31]
	v_pk_fma_f32 v[30:31], v[54:55], v[18:19], v[32:33]
	v_pk_fma_f32 v[32:33], v[50:51], v[22:23], v[60:61]
	v_pk_fma_f32 v[52:53], v[52:53], v[20:21], v[58:59]
	v_cvt_pk_bf16_f32 v30, v30, v31
	v_cvt_pk_bf16_f32 v31, v56, v57
	v_cvt_pk_bf16_f32 v32, v32, v33
	v_lshl_add_u64 v[56:57], s[36:37], 0, v[68:69]
	v_cvt_pk_bf16_f32 v33, v52, v53
	ds_write_b128 v1, v[30:33] offset:64
	ds_read_b128 v[30:33], v15
	ds_read_b128 v[50:53], v28
	v_lshl_add_u64 v[54:55], v[66:67], 0, v[4:5]
	v_lshl_add_u64 v[2:3], v[56:57], 0, v[2:3]
	s_waitcnt lgkmcnt(1)
	global_store_dwordx4 v[26:27], v[30:33], off sc0 sc1
	s_waitcnt lgkmcnt(0)
	global_store_dwordx4 v[54:55], v[50:53], off sc0 sc1
	global_load_dwordx4 v[30:33], v[2:3], off nt
	s_nop 0
	global_load_dwordx4 v[50:53], v[2:3], off offset:16 nt
	global_load_dwordx4 v[240:243], v[2:3], off offset:128 nt
	global_load_dwordx4 v[244:247], v[2:3], off offset:144 nt
	s_waitcnt vmcnt(3)
	v_pk_mul_f32 v[26:27], v[32:33], s[0:1] op_sel_hi:[1,0]
	v_pk_mul_f32 v[30:31], v[30:31], s[0:1] op_sel_hi:[1,0]
	s_waitcnt vmcnt(2)
	v_pk_mul_f32 v[50:51], v[50:51], s[0:1] op_sel_hi:[1,0]
	v_pk_mul_f32 v[32:33], v[52:53], s[0:1] op_sel_hi:[1,0]
	v_pk_fma_f32 v[10:11], v[48:49], v[10:11], v[26:27]
	v_pk_fma_f32 v[12:13], v[46:47], v[12:13], v[30:31]
	v_pk_fma_f32 v[8:9], v[42:43], v[8:9], v[50:51]
	v_pk_fma_f32 v[26:27], v[44:45], v[6:7], v[32:33]
	v_cvt_pk_bf16_f32 v6, v12, v13
	v_cvt_pk_bf16_f32 v7, v10, v11
	v_cvt_pk_bf16_f32 v8, v8, v9
	s_nop 0
	v_cvt_pk_bf16_f32 v9, v26, v27
	s_waitcnt vmcnt(0)
	v_mov_b64_e32 v[10:11], v[240:241]
	v_mov_b64_e32 v[12:13], v[242:243]
	v_mov_b64_e32 v[30:31], v[244:245]
	v_mov_b64_e32 v[32:33], v[246:247]
	ds_write_b128 v1, v[6:9]
	v_add_u32_e32 v2, s1, v25
	v_ashrrev_i32_e32 v3, 31, v2
	v_ashrrev_i32_e32 v25, 31, v24
	v_lshlrev_b64 v[2:3], 12, v[2:3]
	v_lshlrev_b64 v[24:25], 12, v[24:25]
	v_lshl_add_u64 v[2:3], s[12:13], 0, v[2:3]
	v_lshl_add_u64 v[2:3], v[2:3], 0, v[4:5]
	s_waitcnt vmcnt(1)
	v_pk_mul_f32 v[6:7], v[12:13], s[0:1] op_sel_hi:[1,0]
	v_pk_mul_f32 v[8:9], v[10:11], s[0:1] op_sel_hi:[1,0]
	s_waitcnt vmcnt(0)
	v_pk_mul_f32 v[12:13], v[30:31], s[0:1] op_sel_hi:[1,0]
	v_pk_mul_f32 v[10:11], v[32:33], s[0:1] op_sel_hi:[1,0]
	v_pk_fma_f32 v[16:17], v[40:41], v[16:17], v[6:7]
	v_pk_fma_f32 v[6:7], v[38:39], v[18:19], v[8:9]
	v_pk_fma_f32 v[8:9], v[34:35], v[22:23], v[12:13]
	v_pk_fma_f32 v[10:11], v[36:37], v[20:21], v[10:11]
	v_cvt_pk_bf16_f32 v6, v6, v7
	v_cvt_pk_bf16_f32 v7, v16, v17
	v_cvt_pk_bf16_f32 v8, v8, v9
	s_nop 0
	v_cvt_pk_bf16_f32 v9, v10, v11
	ds_write_b128 v1, v[6:9] offset:64
	ds_read_b128 v[6:9], v15
	ds_read_b128 v[10:13], v28
	v_lshl_add_u64 v[14:15], s[12:13], 0, v[24:25]
	v_lshl_add_u64 v[4:5], v[14:15], 0, v[4:5]
	s_waitcnt lgkmcnt(1)
	global_store_dwordx4 v[2:3], v[6:9], off sc0 sc1
	s_waitcnt lgkmcnt(0)
	global_store_dwordx4 v[4:5], v[10:13], off sc0 sc1
	s_waitcnt vmcnt(0)
	s_barrier
